# same as previous + compiler-style 2-state pad between carry-out and carry-in in the regenerated address sequences
# baseline (speedup 1.0000x reference)
.LBB0_1621:
	s_or_b64 exec, exec, s[26:27]
	v_ashrrev_i32_e32 v28, 3, v150
	v_ashrrev_i32_e32 v29, 31, v28
	v_lshl_add_u64 v[6:7], s[42:43], 0, v[28:29]
	v_lshlrev_b32_e32 v5, 3, v150
	v_lshlrev_b64 v[6:7], 11, v[6:7]
	v_and_b32_e32 v10, 56, v5
	v_lshl_add_u64 v[6:7], s[8:9], 0, v[6:7]
	v_lshl_add_u64 v[6:7], v[24:25], 1, v[6:7]
	v_lshlrev_b32_e32 v136, 1, v10
	v_mov_b32_e32 v137, v3
	v_lshl_add_u64 v[8:9], v[6:7], 0, v[136:137]
	v_lshlrev_b32_e32 v27, 8, v4
	v_and_b32_e32 v4, 0xf0, v150
	v_bitop3_b32 v154, v2, v27, v4 bitop3:0xde
	global_load_dwordx4 v[4:7], v[8:9], off offset:128
	v_lshl_add_u64 v[40:41], v[8:9], 0, s[24:25]
	v_add_co_u32_e32 v40, vcc, 0x20000, v40
	s_nop 1
	v_addc_co_u32_e32 v41, vcc, 0, v41, vcc
	global_load_dwordx4 v[20:23], v[40:41], off
	v_add_co_u32_e32 v40, vcc, 0x20000, v40
	s_nop 1
	v_addc_co_u32_e32 v41, vcc, 0, v41, vcc
	global_load_dwordx4 v[116:119], v[40:41], off
	s_movk_i32 s19, 0xf0
	s_waitcnt vmcnt(0)
	v_bitop3_b32 v34, v2, v150, s19 bitop3:0x78
	v_add_u32_e32 v35, 0, v154
	v_add3_u32 v11, v27, v34, 0
	s_and_saveexec_b64 s[26:27], s[38:39]
	s_cbranch_execz .LBB0_1623
	v_lshlrev_b32_e32 v2, 7, v26
	s_waitcnt vmcnt(2)
	ds_write_b128 v35, v[108:111]
	s_waitcnt vmcnt(1)
	ds_write_b128 v11, v[112:115] offset:8192
	ds_write_b128 v35, v[120:123] offset:16384
	ds_write_b128 v11, v[124:127] offset:24576
	ds_write_b128 v35, v[128:131] offset:32768
	ds_write_b128 v11, v[132:135] offset:40960
	s_movk_i32 s20, 0x180
	v_mad_u64_u32 v[40:41], vcc, v26, s20, v[138:139]
	v_mov_b32_e32 v31, v3
	v_lshl_add_u64 v[42:43], v[40:41], 0, v[30:31]
	global_load_dwordx4 v[108:111], v[40:41], off
	global_load_dwordx4 v[112:115], v[42:43], off
	v_mov_b32_e32 v31, v3

.LBB0_3276:
	s_mov_b32 s98, 0xbfb8aa3b
	s_mov_b32 s99, 0xbfb8aa3b
	v_mov_b32_e32 v166, 1.0
	v_mov_b32_e32 v167, 1.0
	v_lshl_add_u32 v140, s64, 8, v143
	s_lshl_b32 s19, s63, 7
	s_and_b32 s19, s19, 0x380
	v_ashrrev_i32_e32 v141, 31, v140
	v_lshlrev_b64 v[168:169], 11, v[140:141]
	v_lshl_add_u64 v[168:169], s[12:13], 0, v[168:169]
	v_or_b32_e32 v2, s19, v152
	v_lshlrev_b32_e32 v2, 1, v2
	v_lshl_add_u64 v[168:169], v[168:169], 0, v[2:3]
	v_pk_mul_f32 v[158:159], v[124:125], s[98:99]
	v_pk_mul_f32 v[160:161], v[126:127], s[98:99]
	v_pk_mul_f32 v[162:163], v[120:121], s[98:99]
	v_pk_mul_f32 v[164:165], v[122:123], s[98:99]
	v_exp_f32_e32 v158, v158
	v_exp_f32_e32 v159, v159
	v_exp_f32_e32 v160, v160
	v_exp_f32_e32 v161, v161
	v_exp_f32_e32 v162, v162
	v_exp_f32_e32 v163, v163
	v_exp_f32_e32 v164, v164
	v_exp_f32_e32 v165, v165
	v_pk_add_f32 v[158:159], v[158:159], v[166:167]
	v_pk_add_f32 v[160:161], v[160:161], v[166:167]
	v_pk_add_f32 v[162:163], v[162:163], v[166:167]
	v_pk_add_f32 v[164:165], v[164:165], v[166:167]
	v_rcp_f32_e32 v158, v158
	v_rcp_f32_e32 v159, v159
	v_rcp_f32_e32 v160, v160
	v_rcp_f32_e32 v161, v161
	v_rcp_f32_e32 v162, v162
	v_rcp_f32_e32 v163, v163
	v_rcp_f32_e32 v164, v164
	v_rcp_f32_e32 v165, v165
	v_pk_mul_f32 v[158:159], v[124:125], v[158:159]
	v_pk_mul_f32 v[160:161], v[126:127], v[160:161]
	v_pk_mul_f32 v[162:163], v[120:121], v[162:163]
	v_pk_mul_f32 v[164:165], v[122:123], v[164:165]
	v_pk_mul_f32 v[158:159], v[128:129], v[158:159]
	v_pk_mul_f32 v[160:161], v[130:131], v[160:161]
	v_pk_mul_f32 v[162:163], v[116:117], v[162:163]
	v_pk_mul_f32 v[164:165], v[118:119], v[164:165]
	v_cvt_pk_bf16_f32 v124, v158, v159
	v_cvt_pk_bf16_f32 v125, v160, v161
	v_cvt_pk_bf16_f32 v126, v162, v163
	v_cvt_pk_bf16_f32 v127, v164, v165
	global_store_dwordx4 v[168:169], v[124:127], off
	v_pk_mul_f32 v[158:159], v[112:113], s[98:99]
	v_pk_mul_f32 v[160:161], v[114:115], s[98:99]
	v_pk_mul_f32 v[162:163], v[104:105], s[98:99]
	v_pk_mul_f32 v[164:165], v[106:107], s[98:99]
	v_exp_f32_e32 v158, v158
	v_exp_f32_e32 v159, v159
	v_exp_f32_e32 v160, v160
	v_exp_f32_e32 v161, v161
	v_exp_f32_e32 v162, v162
	v_exp_f32_e32 v163, v163
	v_exp_f32_e32 v164, v164
	v_exp_f32_e32 v165, v165
	v_pk_add_f32 v[158:159], v[158:159], v[166:167]
	v_pk_add_f32 v[160:161], v[160:161], v[166:167]
	v_pk_add_f32 v[162:163], v[162:163], v[166:167]
	v_pk_add_f32 v[164:165], v[164:165], v[166:167]
	v_rcp_f32_e32 v158, v158
	v_rcp_f32_e32 v159, v159
	v_rcp_f32_e32 v160, v160
	v_rcp_f32_e32 v161, v161
	v_rcp_f32_e32 v162, v162
	v_rcp_f32_e32 v163, v163
	v_rcp_f32_e32 v164, v164
	v_rcp_f32_e32 v165, v165
	v_pk_mul_f32 v[158:159], v[112:113], v[158:159]
	v_pk_mul_f32 v[160:161], v[114:115], v[160:161]
	v_pk_mul_f32 v[162:163], v[104:105], v[162:163]
	v_pk_mul_f32 v[164:165], v[106:107], v[164:165]
	v_pk_mul_f32 v[158:159], v[108:109], v[158:159]
	v_pk_mul_f32 v[160:161], v[110:111], v[160:161]
	v_pk_mul_f32 v[162:163], v[100:101], v[162:163]
	v_pk_mul_f32 v[164:165], v[102:103], v[164:165]
	v_cvt_pk_bf16_f32 v112, v158, v159
	v_cvt_pk_bf16_f32 v113, v160, v161
	v_cvt_pk_bf16_f32 v114, v162, v163
	v_cvt_pk_bf16_f32 v115, v164, v165
	v_add_co_u32_e32 v108, vcc, 0x8000, v168
	s_nop 1
	v_addc_co_u32_e32 v109, vcc, 0, v169, vcc
	global_store_dwordx4 v[108:109], v[112:115], off
	v_pk_mul_f32 v[158:159], v[96:97], s[98:99]
	v_pk_mul_f32 v[160:161], v[98:99], s[98:99]
	v_pk_mul_f32 v[162:163], v[88:89], s[98:99]
	v_pk_mul_f32 v[164:165], v[90:91], s[98:99]
	v_exp_f32_e32 v158, v158
	v_exp_f32_e32 v159, v159
	v_exp_f32_e32 v160, v160
	v_exp_f32_e32 v161, v161
	v_exp_f32_e32 v162, v162
	v_exp_f32_e32 v163, v163
	v_exp_f32_e32 v164, v164
	v_exp_f32_e32 v165, v165
	v_pk_add_f32 v[158:159], v[158:159], v[166:167]
	v_pk_add_f32 v[160:161], v[160:161], v[166:167]
	v_pk_add_f32 v[162:163], v[162:163], v[166:167]
	v_pk_add_f32 v[164:165], v[164:165], v[166:167]
	v_rcp_f32_e32 v158, v158
	v_rcp_f32_e32 v159, v159
	v_rcp_f32_e32 v160, v160
	v_rcp_f32_e32 v161, v161
	v_rcp_f32_e32 v162, v162
	v_rcp_f32_e32 v163, v163
	v_rcp_f32_e32 v164, v164
	v_rcp_f32_e32 v165, v165
	v_pk_mul_f32 v[158:159], v[96:97], v[158:159]
	v_pk_mul_f32 v[160:161], v[98:99], v[160:161]
	v_pk_mul_f32 v[162:163], v[88:89], v[162:163]
	v_pk_mul_f32 v[164:165], v[90:91], v[164:165]
	v_pk_mul_f32 v[158:159], v[92:93], v[158:159]
	v_pk_mul_f32 v[160:161], v[94:95], v[160:161]
	v_pk_mul_f32 v[162:163], v[84:85], v[162:163]
	v_pk_mul_f32 v[164:165], v[86:87], v[164:165]
	v_cvt_pk_bf16_f32 v96, v158, v159
	v_cvt_pk_bf16_f32 v97, v160, v161
	v_cvt_pk_bf16_f32 v98, v162, v163
	v_cvt_pk_bf16_f32 v99, v164, v165
	v_add_co_u32_e32 v92, vcc, 0x10000, v168
	s_nop 1
	v_addc_co_u32_e32 v93, vcc, 0, v169, vcc
	global_store_dwordx4 v[92:93], v[96:99], off
	v_pk_mul_f32 v[158:159], v[80:81], s[98:99]
	v_pk_mul_f32 v[160:161], v[82:83], s[98:99]
	v_pk_mul_f32 v[162:163], v[72:73], s[98:99]
	v_pk_mul_f32 v[164:165], v[74:75], s[98:99]
	v_exp_f32_e32 v158, v158
	v_exp_f32_e32 v159, v159
	v_exp_f32_e32 v160, v160
	v_exp_f32_e32 v161, v161
	v_exp_f32_e32 v162, v162
	v_exp_f32_e32 v163, v163
	v_exp_f32_e32 v164, v164
	v_exp_f32_e32 v165, v165
	v_pk_add_f32 v[158:159], v[158:159], v[166:167]
	v_pk_add_f32 v[160:161], v[160:161], v[166:167]
	v_pk_add_f32 v[162:163], v[162:163], v[166:167]
	v_pk_add_f32 v[164:165], v[164:165], v[166:167]
	v_rcp_f32_e32 v158, v158
	v_rcp_f32_e32 v159, v159
	v_rcp_f32_e32 v160, v160
	v_rcp_f32_e32 v161, v161
	v_rcp_f32_e32 v162, v162
	v_rcp_f32_e32 v163, v163
	v_rcp_f32_e32 v164, v164
	v_rcp_f32_e32 v165, v165
	v_pk_mul_f32 v[158:159], v[80:81], v[158:159]
	v_pk_mul_f32 v[160:161], v[82:83], v[160:161]
	v_pk_mul_f32 v[162:163], v[72:73], v[162:163]
	v_pk_mul_f32 v[164:165], v[74:75], v[164:165]
	v_pk_mul_f32 v[158:159], v[76:77], v[158:159]
	v_pk_mul_f32 v[160:161], v[78:79], v[160:161]
	v_pk_mul_f32 v[162:163], v[68:69], v[162:163]
	v_pk_mul_f32 v[164:165], v[70:71], v[164:165]
	v_cvt_pk_bf16_f32 v80, v158, v159
	v_cvt_pk_bf16_f32 v81, v160, v161
	v_cvt_pk_bf16_f32 v82, v162, v163
	v_cvt_pk_bf16_f32 v83, v164, v165
	v_add_co_u32_e32 v76, vcc, 0x18000, v168
	s_nop 1
	v_addc_co_u32_e32 v77, vcc, 0, v169, vcc
	global_store_dwordx4 v[76:77], v[80:83], off
	v_pk_mul_f32 v[158:159], v[64:65], s[98:99]
	v_pk_mul_f32 v[160:161], v[66:67], s[98:99]
	v_pk_mul_f32 v[162:163], v[56:57], s[98:99]
	v_pk_mul_f32 v[164:165], v[58:59], s[98:99]
	v_exp_f32_e32 v158, v158
	v_exp_f32_e32 v159, v159
	v_exp_f32_e32 v160, v160
	v_exp_f32_e32 v161, v161
	v_exp_f32_e32 v162, v162
	v_exp_f32_e32 v163, v163
	v_exp_f32_e32 v164, v164
	v_exp_f32_e32 v165, v165
	v_pk_add_f32 v[158:159], v[158:159], v[166:167]
	v_pk_add_f32 v[160:161], v[160:161], v[166:167]
	v_pk_add_f32 v[162:163], v[162:163], v[166:167]
	v_pk_add_f32 v[164:165], v[164:165], v[166:167]
	v_rcp_f32_e32 v158, v158
	v_rcp_f32_e32 v159, v159
	v_rcp_f32_e32 v160, v160
	v_rcp_f32_e32 v161, v161
	v_rcp_f32_e32 v162, v162
	v_rcp_f32_e32 v163, v163
	v_rcp_f32_e32 v164, v164
	v_rcp_f32_e32 v165, v165
	v_pk_mul_f32 v[158:159], v[64:65], v[158:159]
	v_pk_mul_f32 v[160:161], v[66:67], v[160:161]
	v_pk_mul_f32 v[162:163], v[56:57], v[162:163]
	v_pk_mul_f32 v[164:165], v[58:59], v[164:165]
	v_pk_mul_f32 v[158:159], v[60:61], v[158:159]
	v_pk_mul_f32 v[160:161], v[62:63], v[160:161]
	v_pk_mul_f32 v[162:163], v[52:53], v[162:163]
	v_pk_mul_f32 v[164:165], v[54:55], v[164:165]
	v_cvt_pk_bf16_f32 v64, v158, v159
	v_cvt_pk_bf16_f32 v65, v160, v161
	v_cvt_pk_bf16_f32 v66, v162, v163
	v_cvt_pk_bf16_f32 v67, v164, v165
	v_add_co_u32_e32 v60, vcc, 0x40000, v168
	s_nop 1
	v_addc_co_u32_e32 v61, vcc, 0, v169, vcc
	global_store_dwordx4 v[60:61], v[64:67], off
	v_pk_mul_f32 v[158:159], v[48:49], s[98:99]
	v_pk_mul_f32 v[160:161], v[50:51], s[98:99]
	v_pk_mul_f32 v[162:163], v[40:41], s[98:99]
	v_pk_mul_f32 v[164:165], v[42:43], s[98:99]
	v_exp_f32_e32 v158, v158
	v_exp_f32_e32 v159, v159
	v_exp_f32_e32 v160, v160
	v_exp_f32_e32 v161, v161
	v_exp_f32_e32 v162, v162
	v_exp_f32_e32 v163, v163
	v_exp_f32_e32 v164, v164
	v_exp_f32_e32 v165, v165
	v_pk_add_f32 v[158:159], v[158:159], v[166:167]
	v_pk_add_f32 v[160:161], v[160:161], v[166:167]
	v_pk_add_f32 v[162:163], v[162:163], v[166:167]
	v_pk_add_f32 v[164:165], v[164:165], v[166:167]
	v_rcp_f32_e32 v158, v158
	v_rcp_f32_e32 v159, v159
	v_rcp_f32_e32 v160, v160
	v_rcp_f32_e32 v161, v161
	v_rcp_f32_e32 v162, v162
	v_rcp_f32_e32 v163, v163
	v_rcp_f32_e32 v164, v164
	v_rcp_f32_e32 v165, v165
	v_pk_mul_f32 v[158:159], v[48:49], v[158:159]
	v_pk_mul_f32 v[160:161], v[50:51], v[160:161]
	v_pk_mul_f32 v[162:163], v[40:41], v[162:163]
	v_pk_mul_f32 v[164:165], v[42:43], v[164:165]
	v_pk_mul_f32 v[158:159], v[44:45], v[158:159]
	v_pk_mul_f32 v[160:161], v[46:47], v[160:161]
	v_pk_mul_f32 v[162:163], v[36:37], v[162:163]
	v_pk_mul_f32 v[164:165], v[38:39], v[164:165]
	v_cvt_pk_bf16_f32 v48, v158, v159
	v_cvt_pk_bf16_f32 v49, v160, v161
	v_cvt_pk_bf16_f32 v50, v162, v163
	v_cvt_pk_bf16_f32 v51, v164, v165
	v_add_co_u32_e32 v44, vcc, 0x48000, v168
	s_nop 1
	v_addc_co_u32_e32 v45, vcc, 0, v169, vcc
	global_store_dwordx4 v[44:45], v[48:51], off
	v_pk_mul_f32 v[158:159], v[32:33], s[98:99]
	v_pk_mul_f32 v[160:161], v[34:35], s[98:99]
	v_pk_mul_f32 v[162:163], v[24:25], s[98:99]
	v_pk_mul_f32 v[164:165], v[26:27], s[98:99]
	v_exp_f32_e32 v158, v158
	v_exp_f32_e32 v159, v159
	v_exp_f32_e32 v160, v160
	v_exp_f32_e32 v161, v161
	v_exp_f32_e32 v162, v162
	v_exp_f32_e32 v163, v163
	v_exp_f32_e32 v164, v164
	v_exp_f32_e32 v165, v165
	v_pk_add_f32 v[158:159], v[158:159], v[166:167]
	v_pk_add_f32 v[160:161], v[160:161], v[166:167]
	v_pk_add_f32 v[162:163], v[162:163], v[166:167]
	v_pk_add_f32 v[164:165], v[164:165], v[166:167]
	v_rcp_f32_e32 v158, v158
	v_rcp_f32_e32 v159, v159
	v_rcp_f32_e32 v160, v160
	v_rcp_f32_e32 v161, v161
	v_rcp_f32_e32 v162, v162
	v_rcp_f32_e32 v163, v163
	v_rcp_f32_e32 v164, v164
	v_rcp_f32_e32 v165, v165
	v_pk_mul_f32 v[158:159], v[32:33], v[158:159]
	v_pk_mul_f32 v[160:161], v[34:35], v[160:161]
	v_pk_mul_f32 v[162:163], v[24:25], v[162:163]
	v_pk_mul_f32 v[164:165], v[26:27], v[164:165]
	v_pk_mul_f32 v[158:159], v[28:29], v[158:159]
	v_pk_mul_f32 v[160:161], v[30:31], v[160:161]
	v_pk_mul_f32 v[162:163], v[20:21], v[162:163]
	v_pk_mul_f32 v[164:165], v[22:23], v[164:165]
	v_cvt_pk_bf16_f32 v32, v158, v159
	v_cvt_pk_bf16_f32 v33, v160, v161
	v_cvt_pk_bf16_f32 v34, v162, v163
	v_cvt_pk_bf16_f32 v35, v164, v165
	v_add_co_u32_e32 v28, vcc, 0x50000, v168
	s_nop 1
	v_addc_co_u32_e32 v29, vcc, 0, v169, vcc
	global_store_dwordx4 v[28:29], v[32:35], off
	v_pk_mul_f32 v[158:159], v[16:17], s[98:99]
	v_pk_mul_f32 v[160:161], v[18:19], s[98:99]
	v_pk_mul_f32 v[162:163], v[8:9], s[98:99]
	v_pk_mul_f32 v[164:165], v[10:11], s[98:99]
	v_exp_f32_e32 v158, v158
	v_exp_f32_e32 v159, v159
	v_exp_f32_e32 v160, v160
	v_exp_f32_e32 v161, v161
	v_exp_f32_e32 v162, v162
	v_exp_f32_e32 v163, v163
	v_exp_f32_e32 v164, v164
	v_exp_f32_e32 v165, v165
	v_pk_add_f32 v[158:159], v[158:159], v[166:167]
	v_pk_add_f32 v[160:161], v[160:161], v[166:167]
	v_pk_add_f32 v[162:163], v[162:163], v[166:167]
	v_pk_add_f32 v[164:165], v[164:165], v[166:167]
	v_rcp_f32_e32 v158, v158
	v_rcp_f32_e32 v159, v159
	v_rcp_f32_e32 v160, v160
	v_rcp_f32_e32 v161, v161
	v_rcp_f32_e32 v162, v162
	v_rcp_f32_e32 v163, v163
	v_rcp_f32_e32 v164, v164
	v_rcp_f32_e32 v165, v165
	v_pk_mul_f32 v[158:159], v[16:17], v[158:159]
	v_pk_mul_f32 v[160:161], v[18:19], v[160:161]
	v_pk_mul_f32 v[162:163], v[8:9], v[162:163]
	v_pk_mul_f32 v[164:165], v[10:11], v[164:165]
	v_pk_mul_f32 v[158:159], v[12:13], v[158:159]
	v_pk_mul_f32 v[160:161], v[14:15], v[160:161]
	v_pk_mul_f32 v[162:163], v[4:5], v[162:163]
	v_pk_mul_f32 v[164:165], v[6:7], v[164:165]
	v_cvt_pk_bf16_f32 v16, v158, v159
	v_cvt_pk_bf16_f32 v17, v160, v161
	v_cvt_pk_bf16_f32 v18, v162, v163
	v_cvt_pk_bf16_f32 v19, v164, v165
	v_add_co_u32_e32 v12, vcc, 0x58000, v168
	s_nop 1
	v_addc_co_u32_e32 v13, vcc, 0, v169, vcc
	global_store_dwordx4 v[12:13], v[16:19], off
	s_and_b64 vcc, exec, s[38:39]
	s_cbranch_vccnz .LBB0_3281
	s_and_b64 vcc, exec, s[40:41]
	v_mov_b32_e32 v4, v157
	v_mov_b32_e32 v8, v154
	v_mov_b32_e32 v6, v156
	v_mov_b32_e32 v10, v155
	s_cbranch_vccnz .LBB0_3279
	s_waitcnt vmcnt(0)
	v_mad_u64_u32 v[4:5], s[20:21], v142, s48, v[132:133]
	v_mad_u64_u32 v[6:7], s[20:21], v145, s48, v[132:133]
	v_mad_u64_u32 v[8:9], s[20:21], v144, s48, v[134:135]
	v_mad_u64_u32 v[10:11], s[20:21], v146, s48, v[134:135]
